# LDS-DMA staging of all 16 Wv fragments per wave (last two in the wave's own dead qk exchange slots)
# speedup vs baseline: 1.0215x; 1.0215x over previous
.Lring_go_0:
	v_mul_f32_e32 v74, v10, v70
	v_mul_f32_e32 v75, v6, v70
	v_mul_f32_e32 v76, v10, v66
	v_mul_f32_e32 v77, v6, v66
	v_mul_f32_e32 v78, v10, v62
	v_mul_f32_e32 v79, v6, v62
	v_mul_f32_e32 v80, v10, v58
	v_mul_f32_e32 v81, v6, v58
	v_mul_f32_e32 v82, v10, v54
	v_mul_f32_e32 v83, v6, v54
	v_mul_f32_e32 v84, v10, v46
	v_mul_f32_e32 v85, v6, v46
	v_mul_f32_e32 v86, v10, v34
	v_mul_f32_e32 v87, v6, v34
	v_mul_f32_e32 v88, v10, v14
	v_mul_f32_e32 v89, v6, v14
	v_fmac_f32_e32 v74, v71, v11
	v_fmac_f32_e32 v75, v71, v7
	v_fmac_f32_e32 v76, v67, v11
	v_fmac_f32_e32 v77, v67, v7
	v_fmac_f32_e32 v78, v63, v11
	v_fmac_f32_e32 v79, v63, v7
	v_fmac_f32_e32 v80, v59, v11
	v_fmac_f32_e32 v81, v59, v7
	v_fmac_f32_e32 v82, v55, v11
	v_fmac_f32_e32 v83, v55, v7
	v_fmac_f32_e32 v84, v47, v11
	v_fmac_f32_e32 v85, v47, v7
	v_fmac_f32_e32 v86, v35, v11
	v_fmac_f32_e32 v87, v35, v7
	v_fmac_f32_e32 v88, v15, v11
	v_fmac_f32_e32 v89, v15, v7
	v_fmac_f32_e32 v74, v72, v12
	v_fmac_f32_e32 v75, v72, v8
	v_fmac_f32_e32 v76, v68, v12
	v_fmac_f32_e32 v77, v68, v8
	v_fmac_f32_e32 v78, v64, v12
	v_fmac_f32_e32 v79, v64, v8
	v_fmac_f32_e32 v80, v60, v12
	v_fmac_f32_e32 v81, v60, v8
	v_fmac_f32_e32 v82, v56, v12
	v_fmac_f32_e32 v83, v56, v8
	v_fmac_f32_e32 v84, v48, v12
	v_fmac_f32_e32 v85, v48, v8
	v_fmac_f32_e32 v86, v36, v12
	v_fmac_f32_e32 v87, v36, v8
	v_fmac_f32_e32 v88, v16, v12
	v_fmac_f32_e32 v89, v16, v8
	v_fmac_f32_e32 v74, v73, v13
	v_fmac_f32_e32 v75, v73, v9
	v_fmac_f32_e32 v76, v69, v13
	v_fmac_f32_e32 v77, v69, v9
	v_fmac_f32_e32 v78, v65, v13
	v_fmac_f32_e32 v79, v65, v9
	v_fmac_f32_e32 v80, v61, v13
	v_fmac_f32_e32 v81, v61, v9
	v_fmac_f32_e32 v82, v57, v13
	v_fmac_f32_e32 v83, v57, v9
	v_fmac_f32_e32 v84, v49, v13
	v_fmac_f32_e32 v85, v49, v9
	v_fmac_f32_e32 v86, v37, v13
	v_fmac_f32_e32 v87, v37, v9
	v_fmac_f32_e32 v88, v17, v13
	v_fmac_f32_e32 v89, v17, v9
	v_permlane32_swap_b32_e32 v74, v82
	v_permlane32_swap_b32_e32 v75, v83
	v_permlane32_swap_b32_e32 v76, v84
	v_permlane32_swap_b32_e32 v77, v85
	v_permlane32_swap_b32_e32 v78, v86
	v_permlane32_swap_b32_e32 v79, v87
	v_permlane32_swap_b32_e32 v80, v88
	v_permlane32_swap_b32_e32 v81, v89
	v_add_f32_e32 v74, v74, v82
	v_add_f32_e32 v75, v75, v83
	v_add_f32_e32 v76, v76, v84
	v_add_f32_e32 v77, v77, v85
	v_add_f32_e32 v78, v78, v86
	v_add_f32_e32 v79, v79, v87
	v_add_f32_e32 v80, v80, v88
	v_add_f32_e32 v81, v81, v89
	v_permlane16_swap_b32_e32 v74, v78
	v_permlane16_swap_b32_e32 v75, v79
	v_permlane16_swap_b32_e32 v76, v80
	v_permlane16_swap_b32_e32 v77, v81
	v_add_f32_e32 v74, v74, v78
	v_add_f32_e32 v75, v75, v79
	v_add_f32_e32 v76, v76, v80
	v_add_f32_e32 v77, v77, v81
	v_add_f32_dpp v74, v74, v74 row_ror:8 row_mask:0xf bank_mask:0xf bound_ctrl:1
	v_add_f32_dpp v76, v76, v76 row_ror:8 row_mask:0xf bank_mask:0xf bound_ctrl:1
	v_add_f32_dpp v75, v75, v75 row_ror:8 row_mask:0xf bank_mask:0xf bound_ctrl:1
	v_add_f32_dpp v77, v77, v77 row_ror:8 row_mask:0xf bank_mask:0xf bound_ctrl:1
	v_cndmask_b32_e64 v74, v76, v74, s[4:5]
	v_cndmask_b32_e64 v75, v77, v75, s[4:5]
	v_cmp_eq_u32_e64 s[0:1], 0, v107
	v_add_f32_dpp v74, v74, v74 row_half_mirror row_mask:0xf bank_mask:0xf bound_ctrl:1
	v_add_f32_dpp v75, v75, v75 row_half_mirror row_mask:0xf bank_mask:0xf bound_ctrl:1
	v_cndmask_b32_e64 v74, v75, v74, s[2:3]
	s_nop 1
	v_add_f32_dpp v74, v74, v74 quad_perm:[2,3,0,1] row_mask:0xf bank_mask:0xf bound_ctrl:1
	s_nop 1
	v_add_f32_dpp v74, v74, v74 quad_perm:[1,0,3,2] row_mask:0xf bank_mask:0xf bound_ctrl:1
	v_cndmask_b32_e64 v74, v113, v74, s[0:1]
	s_and_saveexec_b64 s[0:1], vcc
	ds_write_b32 v114, v74
	s_or_b64 exec, exec, s[0:1]
	v_mov_b32_dpp v90, v74 row_ror:8 row_mask:0xf bank_mask:0xf bound_ctrl:1
	v_add_u32_e32 v114, 32, v114
	v_max_f32_e32 v90, v74, v90
	v_mov_b32_e32 v91, v90
	s_nop 1
	v_permlane16_swap_b32_e32 v90, v91
	s_nop 0
	v_max_f32_e32 v90, v90, v91
	v_mov_b32_e32 v91, v90
	s_nop 1
	v_permlane32_swap_b32_e32 v90, v91
	s_nop 0
	v_max3_f32 v92, v104, v90, v91
	v_sub_f32_e32 v93, v104, v92
	v_sub_f32_e32 v94, v74, v92
	v_exp_f32_e32 v93, v93
	v_exp_f32_e32 v94, v94
	v_mov_b32_e32 v104, v92
	s_nop 1
	v_fma_f32 v105, v105, v93, v94
	s_nop 0
	v_readlane_b32 s34, v93, 0
	v_readlane_b32 s36, v93, 4
	v_readlane_b32 s38, v94, 0
	v_readlane_b32 s40, v94, 4
	v_readlane_b32 s42, v94, 8
	v_readlane_b32 s44, v94, 12
	v_readlane_b32 s46, v94, 16
	v_readlane_b32 s48, v94, 20
	v_readlane_b32 s50, v94, 24
	v_readlane_b32 s52, v94, 28
	v_readlane_b32 s54, v94, 32
	v_readlane_b32 s56, v94, 36
	v_readlane_b32 s58, v94, 40
	v_readlane_b32 s60, v94, 44
	v_readlane_b32 s62, v94, 48
	v_readlane_b32 s64, v94, 52
	v_readlane_b32 s66, v94, 56
	v_readlane_b32 s68, v94, 60
	s_nop 1
	v_pk_mul_f32 v[96:97], v[96:97], s[34:35] op_sel_hi:[1,0]
	v_pk_mul_f32 v[98:99], v[98:99], s[34:35] op_sel_hi:[1,0]
	v_pk_mul_f32 v[100:101], v[100:101], s[36:37] op_sel_hi:[1,0]
	v_pk_mul_f32 v[102:103], v[102:103], s[36:37] op_sel_hi:[1,0]
	v_pk_fma_f32 v[96:97], v[70:71], s[38:39], v[96:97] op_sel_hi:[1,0,1]
	v_pk_fma_f32 v[98:99], v[72:73], s[38:39], v[98:99] op_sel_hi:[1,0,1]
	v_pk_fma_f32 v[100:101], v[70:71], s[40:41], v[100:101] op_sel_hi:[1,0,1]
	v_pk_fma_f32 v[102:103], v[72:73], s[40:41], v[102:103] op_sel_hi:[1,0,1]
	v_pk_fma_f32 v[96:97], v[66:67], s[42:43], v[96:97] op_sel_hi:[1,0,1]
	v_pk_fma_f32 v[98:99], v[68:69], s[42:43], v[98:99] op_sel_hi:[1,0,1]
	v_pk_fma_f32 v[100:101], v[66:67], s[44:45], v[100:101] op_sel_hi:[1,0,1]
	v_pk_fma_f32 v[102:103], v[68:69], s[44:45], v[102:103] op_sel_hi:[1,0,1]
	v_pk_fma_f32 v[96:97], v[62:63], s[46:47], v[96:97] op_sel_hi:[1,0,1]
	v_pk_fma_f32 v[98:99], v[64:65], s[46:47], v[98:99] op_sel_hi:[1,0,1]
	v_pk_fma_f32 v[100:101], v[62:63], s[48:49], v[100:101] op_sel_hi:[1,0,1]
	v_pk_fma_f32 v[102:103], v[64:65], s[48:49], v[102:103] op_sel_hi:[1,0,1]
	v_pk_fma_f32 v[96:97], v[58:59], s[50:51], v[96:97] op_sel_hi:[1,0,1]
	v_pk_fma_f32 v[98:99], v[60:61], s[50:51], v[98:99] op_sel_hi:[1,0,1]
	v_pk_fma_f32 v[100:101], v[58:59], s[52:53], v[100:101] op_sel_hi:[1,0,1]
	v_pk_fma_f32 v[102:103], v[60:61], s[52:53], v[102:103] op_sel_hi:[1,0,1]
	v_pk_fma_f32 v[96:97], v[54:55], s[54:55], v[96:97] op_sel_hi:[1,0,1]
	v_pk_fma_f32 v[98:99], v[56:57], s[54:55], v[98:99] op_sel_hi:[1,0,1]
	v_pk_fma_f32 v[100:101], v[54:55], s[56:57], v[100:101] op_sel_hi:[1,0,1]
	v_pk_fma_f32 v[102:103], v[56:57], s[56:57], v[102:103] op_sel_hi:[1,0,1]
	v_pk_fma_f32 v[96:97], v[46:47], s[58:59], v[96:97] op_sel_hi:[1,0,1]
	v_pk_fma_f32 v[98:99], v[48:49], s[58:59], v[98:99] op_sel_hi:[1,0,1]
	v_pk_fma_f32 v[100:101], v[46:47], s[60:61], v[100:101] op_sel_hi:[1,0,1]
	v_pk_fma_f32 v[102:103], v[48:49], s[60:61], v[102:103] op_sel_hi:[1,0,1]
	v_pk_fma_f32 v[96:97], v[34:35], s[62:63], v[96:97] op_sel_hi:[1,0,1]
	v_pk_fma_f32 v[98:99], v[36:37], s[62:63], v[98:99] op_sel_hi:[1,0,1]
	v_pk_fma_f32 v[100:101], v[34:35], s[64:65], v[100:101] op_sel_hi:[1,0,1]
	v_pk_fma_f32 v[102:103], v[36:37], s[64:65], v[102:103] op_sel_hi:[1,0,1]
	v_pk_fma_f32 v[96:97], v[14:15], s[66:67], v[96:97] op_sel_hi:[1,0,1]
	v_pk_fma_f32 v[98:99], v[16:17], s[66:67], v[98:99] op_sel_hi:[1,0,1]
	v_pk_fma_f32 v[100:101], v[14:15], s[68:69], v[100:101] op_sel_hi:[1,0,1]
	v_pk_fma_f32 v[102:103], v[16:17], s[68:69], v[102:103] op_sel_hi:[1,0,1]
	s_cmp_lg_u32 s30, 8
	s_cbranch_scc1 .Lring_nostage
	v_lshlrev_b32_e32 v176, 4, v196
	v_lshl_add_u32 v176, v197, 14, v176
	s_mov_b32 m0, s33
	s_nop 0
	global_load_lds_dwordx4 v176, s[8:9]
	global_load_lds_dwordx4 v176, s[8:9] offset:1024
	global_load_lds_dwordx4 v176, s[8:9] offset:2048
	global_load_lds_dwordx4 v176, s[8:9] offset:3072
	v_add_u32_e32 v176, 0x1000, v176
	s_add_u32 s35, s33, 4096
	s_mov_b32 m0, s35
	s_nop 0
	global_load_lds_dwordx4 v176, s[8:9]
	global_load_lds_dwordx4 v176, s[8:9] offset:1024
	global_load_lds_dwordx4 v176, s[8:9] offset:2048
	global_load_lds_dwordx4 v176, s[8:9] offset:3072
	v_add_u32_e32 v176, 0x1000, v176
	s_add_u32 s35, s33, 8192
	s_mov_b32 m0, s35
	s_nop 0
	global_load_lds_dwordx4 v176, s[8:9]
	global_load_lds_dwordx4 v176, s[8:9] offset:1024
	global_load_lds_dwordx4 v176, s[8:9] offset:2048
	v_add_u32_e32 v176, 0xc00, v176
	s_mul_i32 s35, s32, 3072
	s_add_u32 s35, s35, 46080
	s_mov_b32 m0, s35
	s_nop 0
	global_load_lds_dwordx4 v176, s[8:9]
	global_load_lds_dwordx4 v176, s[8:9] offset:1024
	global_load_lds_dwordx4 v176, s[8:9] offset:2048
	v_add_u32_e32 v176, 0xc00, v176
	s_mul_i32 s35, s32, 2048
	s_add_u32 s35, s35, 16640
	s_mov_b32 m0, s35
	s_nop 0
	global_load_lds_dwordx4 v176, s[8:9]
	global_load_lds_dwordx4 v176, s[8:9] offset:1024

.Lring_done:
	s_setprio 0
	v_mov_b32_e32 v240, v96
	v_mov_b32_e32 v241, v97
	v_mov_b32_e32 v242, v98
	v_mov_b32_e32 v243, v99
	v_mov_b32_e32 v244, v100
	v_mov_b32_e32 v245, v101
	v_mov_b32_e32 v246, v102
	v_mov_b32_e32 v247, v103
	v_mov_b32_e32 v248, v104
	v_mov_b32_e32 v249, v105
	s_movk_i32 s0, 0x640
	v_mov_b32_e32 v14, 0x8200
	v_mad_u32_u24 v205, v197, s0, v14
	v_lshlrev_b32_e32 v10, 4, v106
	v_or_b32_e32 v6, 0x2000, v196
	v_add_lshl_u32 v7, v122, v6, 4
	v_lshlrev_b32_e32 v11, 4, v196
	v_add_u32_e32 v11, s33, v11
	s_mul_i32 s35, s32, 3072
	s_add_u32 s35, s35, 46080
	v_lshlrev_b32_e32 v12, 4, v196
	v_add_u32_e32 v12, s35, v12
	s_mul_i32 s35, s32, 2048
	s_add_u32 s35, s35, 16640
	v_lshlrev_b32_e32 v13, 4, v196
	s_nop 0
	v_add_u32_e32 v13, s35, v13
	ds_read_b128 v[158:161], v11
	ds_read_b128 v[154:157], v11 offset:1024
	ds_read_b128 v[146:149], v11 offset:2048
	ds_read_b128 v[138:141], v11 offset:3072
	ds_read_b128 v[118:121], v11 offset:4096
	ds_read_b128 v[106:109], v11 offset:5120
	ds_read_b128 v[98:101], v11 offset:6144
	ds_read_b128 v[102:105], v11 offset:7168
	ds_read_b128 v[170:173], v11 offset:8192
	ds_read_b128 v[166:169], v11 offset:9216
	ds_read_b128 v[178:181], v11 offset:10240
	ds_read_b128 v[174:177], v12
	ds_read_b128 v[162:165], v12 offset:1024
	s_nop 0
	ds_read_b128 v[134:137], v12 offset:2048
	ds_read_b128 v[114:117], v13
	ds_read_b128 v[110:113], v13 offset:1024
	global_load_dwordx4 v[94:97], v7, s[8:9]
	global_load_dwordx4 v[90:93], v7, s[8:9] offset:1024
	global_load_dwordx4 v[78:81], v7, s[8:9] offset:2048
	global_load_dwordx4 v[74:77], v7, s[8:9] offset:3072
	v_add_lshl_u32 v7, v123, v6, 4
	v_add_lshl_u32 v8, v124, v6, 4
	global_load_dwordx4 v[66:69], v7, s[8:9]
	global_load_dwordx4 v[58:61], v8, s[8:9]
	v_add_lshl_u32 v7, v125, v6, 4
	v_add_lshl_u32 v8, v126, v6, 4
	global_load_dwordx4 v[62:65], v7, s[8:9]
	global_load_dwordx4 v[54:57], v8, s[8:9]
	v_add_lshl_u32 v7, v127, v6, 4
	v_add_lshl_u32 v8, v128, v6, 4
	global_load_dwordx4 v[150:153], v7, s[8:9]
	global_load_dwordx4 v[142:145], v8, s[8:9]
	v_add_lshl_u32 v7, v129, v6, 4
	v_add_lshl_u32 v8, v130, v6, 4
	global_load_dwordx4 v[130:133], v7, s[8:9]
	global_load_dwordx4 v[126:129], v8, s[8:9]
	v_add_lshl_u32 v7, v192, v6, 4
	v_add_lshl_u32 v8, v202, v6, 4
	global_load_dwordx4 v[122:125], v7, s[8:9]
	global_load_dwordx4 v[82:85], v8, s[8:9]
	v_add_lshl_u32 v7, v203, v6, 4
	v_add_lshl_u32 v6, v204, v6, 4
	global_load_dwordx4 v[86:89], v7, s[8:9]
	global_load_dwordx4 v[70:73], v6, s[8:9]
	v_lshlrev_b32_e32 v187, 2, v195
	v_and_or_b32 v190, v187, 4, s31
	v_or_b32_e32 v208, 1, v190
	v_mul_u32_u24_e32 v6, 0x300, v197
	v_ashrrev_i32_e32 v191, 31, v190
	v_ashrrev_i32_e32 v209, 31, v208
	v_or_b32_e32 v6, v196, v6
	v_lshlrev_b64 v[210:211], 9, v[190:191]
	v_lshlrev_b32_e32 v191, 2, v1
	v_lshlrev_b64 v[222:223], 9, v[208:209]
	v_or_b32_e32 v208, 2, v190
	v_mov_b32_e32 v193, 0
	v_lshlrev_b32_e32 v14, 4, v6
	v_lshl_or_b32 v192, v197, 7, v191
	s_movk_i32 s2, 0xfe00
	v_ashrrev_i32_e32 v209, 31, v208
	v_or_b32_e32 v6, 0x40000, v14
	s_movk_i32 s1, 0x100
	v_lshl_add_u64 v[220:221], s[22:23], 0, v[192:193]
	s_mov_b32 s3, -1
	v_lshlrev_b64 v[226:227], 9, v[208:209]
	v_or_b32_e32 v208, 3, v190
	global_load_dwordx4 v[50:53], v6, s[8:9]
	global_load_dwordx4 v[46:49], v6, s[8:9] offset:1024
	global_load_dwordx4 v[42:45], v6, s[8:9] offset:2048
	global_load_dwordx4 v[30:33], v6, s[8:9] offset:3072
	v_add_u32_e32 v6, 0x41000, v14
	v_add_u32_e32 v7, 0x41400, v14
	v_lshl_add_u64 v[212:213], s[20:21], 0, v[192:193]
	v_lshl_add_u64 v[202:203], v[220:221], 0, s[2:3]
	v_cmp_gt_u32_e32 vcc, s1, v0
	v_ashrrev_i32_e32 v209, 31, v208
	s_movk_i32 s2, 0xfe40
	global_load_dwordx4 v[38:41], v6, s[8:9]
	global_load_dwordx4 v[22:25], v7, s[8:9]
	v_add_u32_e32 v6, 0x41800, v14
	v_add_u32_e32 v7, 0x41c00, v14
	v_cndmask_b32_e32 v203, v203, v213, vcc
	v_cndmask_b32_e32 v202, v202, v212, vcc
	v_lshlrev_b64 v[230:231], 9, v[208:209]
	s_mov_b32 s3, -1
	global_load_dwordx4 v[34:37], v6, s[8:9]
	global_load_dwordx4 v[10:13], v7, s[8:9]
	v_add_u32_e32 v6, 0x42000, v14
	v_add_u32_e32 v7, 0x42400, v14
	v_add_u32_e32 v15, 0x42800, v14
	v_add_u32_e32 v18, 0x42c00, v14
	v_lshl_add_u64 v[206:207], v[202:203], 0, v[210:211]
	v_lshl_add_u64 v[224:225], v[202:203], 0, v[222:223]
	v_lshl_add_u64 v[228:229], v[202:203], 0, v[226:227]
	v_lshl_add_u64 v[202:203], v[202:203], 0, v[230:231]
	v_lshl_add_u64 v[212:213], v[212:213], 0, 64
	v_lshl_add_u64 v[220:221], v[220:221], 0, s[2:3]
	global_load_dwordx4 v[26:29], v6, s[8:9]
	s_nop 0
	global_load_dwordx4 v[6:9], v7, s[8:9]
	s_nop 0
	global_load_dwordx4 v[14:17], v15, s[8:9]
	s_nop 0
	global_load_dwordx4 v[18:21], v18, s[8:9]
	s_nop 0
	global_load_dword v208, v[206:207], off
	s_nop 0
	global_load_dword v207, v[224:225], off
	global_load_dword v204, v[228:229], off
	s_nop 0
	global_load_dword v203, v[202:203], off
	s_nop 0
	global_load_dword v206, v192, s[10:11]
	global_load_dword v202, v192, s[10:11] offset:64
	v_cndmask_b32_e32 v213, v221, v213, vcc
	v_cndmask_b32_e32 v212, v220, v212, vcc
	v_lshl_add_u64 v[210:211], v[212:213], 0, v[210:211]
	v_lshl_add_u64 v[220:221], v[212:213], 0, v[222:223]
	v_lshl_add_u64 v[222:223], v[212:213], 0, v[226:227]
	v_lshl_add_u64 v[224:225], v[212:213], 0, v[230:231]
	global_load_dword v212, v[210:211], off
	s_nop 0
	global_load_dword v211, v[220:221], off
	global_load_dword v210, v[222:223], off
	global_load_dword v209, v[224:225], off
	v_lshl_or_b32 v190, v197, 4, v1
	v_lshlrev_b32_e32 v186, 2, v190
	global_load_dword v189, v186, s[24:25]
	global_load_dword v188, v186, s[26:27]
	v_mov_b32_e32 v233, v249
	v_mov_b32_e32 v232, v248
	v_mov_b32_e32 v214, v240
	v_mov_b32_e32 v215, v241
	v_mov_b32_e32 v216, v242
	v_mov_b32_e32 v217, v243
	v_mov_b32_e32 v218, v244
	v_mov_b32_e32 v219, v245
	v_mov_b32_e32 v220, v246
	v_mov_b32_e32 v221, v247
	s_nop 1
	v_add_f32_dpp v2, v233, v233 row_ror:8 row_mask:0xf bank_mask:0xf bound_ctrl:1
	v_mov_b32_e32 v3, v2
	s_nop 1
	v_permlane16_swap_b32_e32 v2, v3
	v_add_f32_e32 v2, v2, v3
	v_mov_b32_e32 v3, v2
	s_nop 1
	v_permlane32_swap_b32_e32 v2, v3
	v_add_f32_e32 v2, v2, v3
	v_readlane_b32 s2, v232, 4
	v_readlane_b32 s4, v2, 4
	v_readlane_b32 s5, v2, 0
	v_readlane_b32 s3, v232, 0
	v_div_scale_f32 v3, s[0:1], s4, s4, 1.0
	v_rcp_f32_e32 v4, v3
	v_lshl_add_u64 v[182:183], v[182:183], 2, s[28:29]
	v_fma_f32 v2, -v3, v4, 1.0
	v_fmac_f32_e32 v4, v2, v4
	v_div_scale_f32 v2, vcc, 1.0, s4, 1.0
	v_mul_f32_e32 v5, v2, v4
	v_fma_f32 v192, -v3, v5, v2
	v_fmac_f32_e32 v5, v192, v4
	v_fma_f32 v2, -v3, v5, v2
	v_div_scale_f32 v3, s[0:1], s5, s5, 1.0
	v_rcp_f32_e32 v192, v3
	v_div_fmas_f32 v2, v2, v4, v5
	v_div_fixup_f32 v2, v2, s4, 1.0
	s_movk_i32 s0, 0xc8
	v_fma_f32 v4, -v3, v192, 1.0
	v_fmac_f32_e32 v192, v4, v192
	v_div_scale_f32 v4, vcc, 1.0, s5, 1.0
	v_mul_f32_e32 v5, v4, v192
	v_fma_f32 v213, -v3, v5, v4
	v_fmac_f32_e32 v5, v213, v192
	v_fma_f32 v3, -v3, v5, v4
	v_div_fmas_f32 v3, v3, v192, v5
	v_div_fixup_f32 v4, v3, s5, 1.0
	v_pk_mul_f32 v[216:217], v[216:217], v[4:5] op_sel_hi:[1,0]
	v_pk_mul_f32 v[214:215], v[214:215], v[4:5] op_sel_hi:[1,0]
	v_cvt_pk_f16_f32 v217, v216, v217
	v_cvt_pk_f16_f32 v216, v214, v215
	v_pk_mul_f32 v[214:215], v[220:221], v[2:3] op_sel_hi:[1,0]
	v_pk_mul_f32 v[218:219], v[218:219], v[2:3] op_sel_hi:[1,0]
	v_add_u32_e32 v3, v205, v184
	ds_read2_b32 v[220:221], v3 offset0:128 offset1:200
	v_cvt_pk_f16_f32 v215, v214, v215
	v_cvt_pk_f16_f32 v214, v218, v219
	ds_read2st64_b32 v[218:219], v3 offset1:1
	v_add_u32_e32 v192, 32, v3
	ds_write2st64_b64 v185, v[216:217], v[214:215] offset1:1
	ds_read2st64_b32 v[214:215], v192 offset0:4 offset1:5
	s_waitcnt lgkmcnt(3)
	v_subrev_f32_e32 v5, s2, v221
	v_exp_f32_e32 v5, v5
	s_waitcnt lgkmcnt(2)
	v_subrev_f32_e32 v185, s3, v218
	v_exp_f32_e32 v185, v185
	s_waitcnt lgkmcnt(0)
	v_subrev_f32_e32 v205, s2, v214
	v_mul_f32_e32 v5, v2, v5
	v_subrev_f32_e32 v192, s3, v219
	v_exp_f32_e32 v205, v205
	v_fmac_f32_e32 v5, v4, v185
	v_mov_b32_e32 v185, v193
	v_exp_f32_e32 v192, v192
	v_lshl_add_u64 v[182:183], v[182:183], 0, v[184:185]
	v_subrev_f32_e32 v185, s2, v215
	v_mul_f32_e32 v5, 0.5, v5
	v_subrev_f32_e32 v184, s3, v220
	v_exp_f32_e32 v185, v185
	global_store_dword v[182:183], v5, off
	v_mul_f32_e32 v5, v2, v205
	v_exp_f32_e32 v184, v184
	v_fmac_f32_e32 v5, v4, v192
	v_mul_f32_e32 v5, 0.5, v5
	global_store_dword v[182:183], v5, off offset:256
	v_mul_f32_e32 v5, v2, v185
	v_fmac_f32_e32 v5, v4, v184
	v_mul_f32_e32 v5, 0.5, v5
	global_store_dword v[182:183], v5, off offset:512
	v_or_b32_e32 v5, 0xc0, v196
	v_cmp_gt_u32_e32 vcc, s0, v5
	s_and_saveexec_b64 s[0:1], vcc
	s_cbranch_execz .LBB1_19
	v_add_u32_e32 v3, 0x300, v3
	ds_read2_b32 v[184:185], v3 offset1:200
	s_waitcnt lgkmcnt(0)
	v_subrev_f32_e32 v3, s3, v184
	v_subrev_f32_e32 v5, s2, v185
	v_exp_f32_e32 v184, v3
	v_exp_f32_e32 v185, v5
	v_mov_b32_e32 v5, v2
	v_pk_mul_f32 v[2:3], v[4:5], v[184:185]
	s_nop 0
	v_add_f32_e32 v2, v2, v3
	v_mul_f32_e32 v2, 0.5, v2
	global_store_dword v[182:183], v2, off offset:768
